# prologue: S5 chunk-matrix items moved from workgroups 0-127 to 128-255 (those have one transposition item fewer), on top of v15
# baseline (speedup 1.0000x reference)
; #define LAS __attribute__((address_space(3)))
; __device__ __forceinline__ void p0_s5_item(const Args& a, unsigned char* ws, LAS unsigned char* lds, int lg, int tid) {
;     LAS float* PWr = (LAS float*)lds; LAS float* PWi = PWr + 17 * 64; LAS float* BBr = PWi + 17 * 64; LAS float* BBi = BBr + 1024; LAS float* CCr = BBi + 1024; LAS float* CCi = CCr + 1024; LAS float* KL = CCi + 1024;
;     bf16* TW = (bf16*)(ws + WS_S5M + (size_t)lg * S5M_STRIDE); bf16* WE = TW + 256 * 384; float* A16 = (float*)(ws + WS_S5M + (size_t)lg * S5M_STRIDE + 196608 + 65536);
;     __syncthreads();
;     if (tid < 64) { const int p = tid;
;         const float are = a.in[5][lg * 64 + p], aim = a.in[6][lg * 64 + p], dt = expf(a.in[7][lg]);
;         float sn, cs; sincosf(aim * dt, &sn, &cs);
;         const float mag = expf(are * dt), abr = mag * cs, abi = mag * sn;
;         const float nr = abr - 1.0f, ni = abi, den = are * are + aim * aim;
;         const float cfr = (nr * are + ni * aim) / den, cfi = (ni * are - nr * aim) / den;
;         for (int m = 0; m < 16; ++m) { const float br = a.in[8][(lg * 64 + p) * 16 + m], bi = a.in[9][(lg * 64 + p) * 16 + m]; BBr[p * 16 + m] = cfr * br - cfi * bi; BBi[p * 16 + m] = cfr * bi + cfi * br; }
;         float wr = 1.f, wi = 0.f;
;         for (int t = 0; t <= 16; ++t) { PWr[t * 64 + p] = wr; PWi[t * 64 + p] = wi; const float nwr = wr * abr - wi * abi, nwi = wr * abi + wi * abr; wr = nwr; wi = nwi; }
;         A16[2 * p] = PWr[16 * 64 + p]; A16[2 * p + 1] = PWi[16 * 64 + p]; }
;     for (int i = tid; i < 1024; i += NTHR) { CCr[i] = a.in[10][lg * 1024 + i]; CCi[i] = a.in[11][lg * 1024 + i]; }
; __device__ __forceinline__ void p0_prologue(const Args& a, LAS unsigned char* lds, int G, int bid) {
;     ...
;     for (int lg = bid; lg < 128; lg += G) p0_s5_item(a, ws, lds, lg, tid);
.LBB0_49:
	s_sub_i32 s100, s72, 0x80
	s_cmp_lt_u32 s100, 0x80
	v_lshlrev_b32_e32 v15, 2, v102
	s_cbranch_scc1 .LBB0_51
	v_lshlrev_b32_e32 v2, 2, v102
	s_cbranch_execz .LBB0_52
	s_branch .LBB0_105
.LBB0_51:
.LBB0_52:
	v_and_b32_e32 v3, 31, v62
	v_lshlrev_b32_e32 v14, 3, v3
	v_not_b32_e32 v3, v62
	v_lshlrev_b32_e32 v3, 5, v3
	v_and_b32_e32 v24, 0x3c0, v3
	v_max_i32_e32 v3, 0x200, v62
	v_sub_u32_e32 v3, v3, v62
	v_add_u32_e32 v3, 0x1ff, v3
	s_load_dwordx8 s[36:43], s[0:1], 0x28
	s_load_dwordx4 s[28:31], s[0:1], 0x48
	s_load_dwordx2 s[56:57], s[0:1], 0x58
	v_lshrrev_b32_e32 v4, 9, v3
	s_movk_i32 s76, 0x1ff
	v_add_u32_e32 v5, 1, v4
	v_add_u32_e32 v4, -1, v4
	v_lshrrev_b32_e32 v6, 1, v4
	v_cmp_lt_u32_e64 s[12:13], s76, v3
	v_and_b32_e32 v3, 0xfffffe, v5
	v_lshlrev_b32_e32 v36, 2, v62
	s_waitcnt lgkmcnt(0)
	s_movk_i32 s6, 0xffc4
	v_add_u32_e32 v6, 1, v6
	v_lshl_add_u32 v25, v3, 9, v62
	v_cmp_ne_u32_e64 s[18:19], v5, v3
	v_add_u32_e32 v3, 0, v36
	v_writelane_b32 v228, s48, 0
	s_add_u32 s74, s54, 0x4d182000
	v_lshl_add_u32 v22, v62, 6, 0
	v_mul_lo_u32 v2, v62, s6
	v_lshlrev_b32_e32 v12, 1, v62
	s_movk_i32 s6, 0x400
	s_movk_i32 s8, 0x1000
	s_movk_i32 s10, 0x2000
	v_and_b32_e32 v34, 3, v6
	v_add_u32_e32 v37, 0x4200, v3
	v_add_u32_e32 v3, 0, v15
	v_writelane_b32 v228, s49, 1
	s_mov_b32 s48, s59
	s_mov_b32 s52, s94
	s_addc_u32 s75, s55, 0
	v_cmp_gt_i32_e64 s[4:5], 64, v62
	v_ashrrev_i32_e32 v13, 31, v12
	v_cmp_gt_i32_e64 s[6:7], s6, v62
	v_cmp_gt_i32_e64 s[8:9], s8, v62
	v_cmp_gt_i32_e64 s[10:11], s10, v62
	v_bfe_u32 v23, v62, 1, 4
	v_mov_b32_e32 v17, 0
	v_add_u32_e32 v63, 0x200, v62
	v_cmp_lt_u32_e64 s[14:15], 5, v4
	v_and_b32_e32 v35, -4, v6
	v_cmp_ne_u32_e64 s[16:17], 0, v34
	s_lshl_b32 s58, s100, 10
	s_lshl_b32 s77, s33, 10
	v_add_u32_e32 v38, 0x2200, v3
	s_mov_b32 s78, 0x3fb8aa3b
	s_mov_b32 s79, 0xc2ce8ed0
	s_mov_b32 s80, 0x42b17218
	s_mov_b32 s81, 0x3c439041
	s_mov_b32 s82, 0xdb629599
	s_mov_b32 s83, 0xf534ddc0
	s_mov_b32 s84, 0xfc2757d1
	s_mov_b32 s85, 0x4e441529
	s_mov_b32 s86, 0xa2f9836e
	s_mov_b32 s87, 0x3fc90fda
	s_mov_b32 s88, 0x3f22f983
	s_mov_b32 s89, 0xbfc90fda
	v_mov_b32_e32 v39, 0x3c0881c4
	v_mov_b32_e32 v40, 0xbab64f3b
	v_mov_b32_e32 v41, 1.0
	s_movk_i32 s90, 0x1f8
	v_add_u32_e32 v42, v22, v2
	s_mov_b64 s[60:61], 0x800
	s_movk_i32 s91, 0xdff
	s_movk_i32 s92, 0x180
	s_movk_i32 s93, 0x1dff
	s_mov_b32 s94, 0x3fffffc0
	s_mov_b64 s[62:63], 0x30000
	v_mov_b32_e32 v43, 0x7f800000
	v_not_b32_e32 v44, 63
	v_not_b32_e32 v45, 31
	v_mov_b32_e32 v46, 0x7fc00000
	s_mov_b32 s64, s100
	s_branch .LBB0_54
